# attention fast loop: K-fragment lgkmcnt waits moved from the head of the half-step down to their first consuming QK MFMA (on top of SrcC init change)
# baseline (speedup 1.0000x reference)
; #define AT_PK4(P, BASE, OUT) do { u32x4 w = {cvt_pk_bf16(P[BASE + 0], P[BASE + 1]), cvt_pk_bf16(P[BASE + 2], P[BASE + 3]), cvt_pk_bf16(P[BASE + 4], P[BASE + 5]), cvt_pk_bf16(P[BASE + 6], P[BASE + 7])}; \
;     OUT = *reinterpret_cast<bf16x8*>(&w); } while (0)
; __device__ __forceinline__ void finishFast(f32x16& p0, f32x16& p1, bool& ovf, float& l_reg, bf16x8& pa0, bf16x8& pa1, bf16x8& pa2, bf16x8& pa3) {
;     expSM(p1);
;     typedef float f32x2_t __attribute__((ext_vector_type(2)));
;     f32x2_t sa = {p0[0], p0[1]}, sb = {p0[8], p0[9]}, sc = {p1[0], p1[1]}, sd = {p1[8], p1[9]};
; #pragma unroll
;     for (int r = 2; r < 8; r += 2) { sa += f32x2_t{p0[r], p0[r + 1]}; sb += f32x2_t{p0[8 + r], p0[9 + r]}; sc += f32x2_t{p1[r], p1[r + 1]}; sd += f32x2_t{p1[8 + r], p1[9 + r]}; }
;     const f32x2_t ps2 = (sa + sb) + (sc + sd);
;     float ps = ps2.x + ps2.y;
;     { auto rr = __builtin_amdgcn_permlane32_swap(__float_as_uint(ps), __float_as_uint(ps), false, false);
;       ps = __uint_as_float(rr[0]) + __uint_as_float(rr[1]); }
;     l_reg += ps;
;     ...
;     AT_PK4(p0, 0, pa0); AT_PK4(p0, 8, pa1); AT_PK4(p1, 0, pa2); AT_PK4(p1, 8, pa3);
.LBB0_386:
	s_mov_b32 s7, s1
	v_add_u32_e32 v67, s7, v171
	ds_read_b128 v[206:209], v67 offset:0
	ds_read_b128 v[210:213], v67 offset:0x1000
	v_add_u32_e32 v130, s7, v199
	ds_read_b128 v[214:217], v130 offset:0
	ds_read_b128 v[218:221], v130 offset:0x1000
	v_add_u32_e32 v131, s7, v200
	ds_read_b128 v[222:225], v131 offset:0
	ds_read_b128 v[246:249], v131 offset:0x1000
	v_add_u32_e32 v132, s7, v201
	ds_read_b128 v[238:241], v132 offset:0
	ds_read_b128 v[242:245], v132 offset:0x1000
	s_mov_b32 s1, s8
	v_mfma_f32_32x32x16_bf16 v[50:65], v[68:71], v[126:129], v[50:65]
	v_add_f32_e64 v68, v178, v80
	v_add_f32_e64 v69, v179, v81
	v_add_f32_e64 v70, v184, v186
	v_add_f32_e64 v71, v185, v187
	v_add_f32_e64 v68, v180, v68
	v_add_f32_e64 v69, v181, v69
	v_mfma_f32_32x32x16_bf16 v[50:65], v[72:75], v[122:125], v[50:65]
	v_exp_f32_e32 v72, v98
	v_exp_f32_e32 v73, v99
	v_exp_f32_e32 v98, v102
	v_exp_f32_e32 v99, v103
	v_exp_f32_e32 v102, v106
	v_exp_f32_e32 v103, v107
	v_exp_f32_e32 v106, v110
	v_mfma_f32_32x32x16_bf16 v[50:65], v[76:79], v[118:121], v[50:65]
	v_exp_f32_e32 v76, v100
	v_exp_f32_e32 v77, v101
	v_exp_f32_e32 v100, v104
	v_exp_f32_e32 v101, v105
	v_exp_f32_e32 v104, v108
	v_exp_f32_e32 v105, v109
	v_exp_f32_e32 v107, v111
	v_mfma_f32_32x32x16_bf16 v[50:65], v[114:117], v[164:167], v[50:65]
	v_exp_f32_e32 v108, v112
	v_exp_f32_e32 v109, v113
	v_pk_add_f32 v[74:75], v[76:77], v[72:73]
	v_pk_add_f32 v[78:79], v[104:105], v[102:103]
	v_pk_add_f32 v[70:71], v[188:189], v[70:71]
	v_pk_add_f32 v[74:75], v[98:99], v[74:75]
	v_pk_add_f32 v[78:79], v[106:107], v[78:79]
	s_waitcnt lgkmcnt(6)
	v_mfma_f32_32x32x16_bf16 v[130:145], v[206:209], v[148:151], v[82:97]
	v_add_f32_e64 v68, v182, v68
	v_add_f32_e64 v69, v183, v69
	v_add_f32_e64 v70, v190, v70
	v_add_f32_e64 v71, v191, v71
	v_add_f32_e64 v74, v100, v74
	v_add_f32_e64 v75, v101, v75
	v_pk_add_f32 v[78:79], v[108:109], v[78:79]
	v_pk_add_f32 v[68:69], v[70:71], v[68:69]
	v_pk_add_f32 v[70:71], v[74:75], v[78:79]
	v_mfma_f32_32x32x16_bf16 v[114:129], v[210:213], v[148:151], v[82:97]
	v_add_f32_e64 v68, v68, v70
	v_add_f32_e64 v69, v69, v71
	v_add_f32_e64 v176, v68, v69
	v_add_f32_e64 v177, v69, v68
	v_cvt_pk_bf16_f32 v68, v80, v81
	v_cvt_pk_bf16_f32 v69, v178, v179
	v_cvt_pk_bf16_f32 v70, v180, v181
	v_cvt_pk_bf16_f32 v71, v182, v183
	s_waitcnt lgkmcnt(4)
	v_mfma_f32_32x32x16_bf16 v[130:145], v[214:217], v[152:155], v[130:145]
	v_mov_b32_e32 v146, v176
	s_nop 1
	v_permlane32_swap_b32_e32 v176, v146
	v_cvt_pk_bf16_f32 v78, v184, v185
	v_cvt_pk_bf16_f32 v79, v186, v187
	v_cvt_pk_bf16_f32 v80, v188, v189
	v_cvt_pk_bf16_f32 v81, v190, v191
	v_mfma_f32_32x32x16_bf16 v[114:129], v[218:221], v[152:155], v[114:129]
	v_cvt_pk_bf16_f32 v74, v72, v73
	v_cvt_pk_bf16_f32 v75, v76, v77
	v_cvt_pk_bf16_f32 v76, v98, v99
	v_cvt_pk_bf16_f32 v77, v100, v101
	v_cvt_pk_bf16_f32 v98, v102, v103
	v_cvt_pk_bf16_f32 v99, v104, v105
	v_cvt_pk_bf16_f32 v100, v106, v107
	s_waitcnt lgkmcnt(2)
	v_mfma_f32_32x32x16_bf16 v[130:145], v[222:225], v[156:159], v[130:145]
	v_cvt_pk_bf16_f32 v101, v108, v109
	v_mfma_f32_32x32x16_bf16 v[114:129], v[246:249], v[156:159], v[114:129]
	s_waitcnt lgkmcnt(0)
	v_mfma_f32_32x32x16_bf16 v[130:145], v[238:241], v[160:163], v[130:145]
	v_mfma_f32_32x32x16_bf16 v[114:129], v[242:245], v[160:163], v[114:129]
	s_and_b64 vcc, exec, s[42:43]
	s_cbranch_vccnz .LBB0_393
	s_cmp_ge_u32 s2, s65
	s_mov_b64 s[8:9], -1
	s_cbranch_scc0 .LBB0_389
	s_waitcnt vmcnt(0) lgkmcnt(0)
	s_mov_b64 s[8:9], 0

; #define AT_PK4(P, BASE, OUT) do { u32x4 w = {cvt_pk_bf16(P[BASE + 0], P[BASE + 1]), cvt_pk_bf16(P[BASE + 2], P[BASE + 3]), cvt_pk_bf16(P[BASE + 4], P[BASE + 5]), cvt_pk_bf16(P[BASE + 6], P[BASE + 7])}; \
;     OUT = *reinterpret_cast<bf16x8*>(&w); } while (0)
; __device__ __forceinline__ void finishFast(f32x16& p0, f32x16& p1, bool& ovf, float& l_reg, bf16x8& pa0, bf16x8& pa1, bf16x8& pa2, bf16x8& pa3) {
;     expSM(p1);
;     typedef float f32x2_t __attribute__((ext_vector_type(2)));
;     f32x2_t sa = {p0[0], p0[1]}, sb = {p0[8], p0[9]}, sc = {p1[0], p1[1]}, sd = {p1[8], p1[9]};
; #pragma unroll
;     for (int r = 2; r < 8; r += 2) { sa += f32x2_t{p0[r], p0[r + 1]}; sb += f32x2_t{p0[8 + r], p0[9 + r]}; sc += f32x2_t{p1[r], p1[r + 1]}; sd += f32x2_t{p1[8 + r], p1[9 + r]}; }
;     const f32x2_t ps2 = (sa + sb) + (sc + sd);
;     float ps = ps2.x + ps2.y;
;     { auto rr = __builtin_amdgcn_permlane32_swap(__float_as_uint(ps), __float_as_uint(ps), false, false);
;       ps = __uint_as_float(rr[0]) + __uint_as_float(rr[1]); }
;     l_reg += ps;
;     ...
;     AT_PK4(p0, 0, pa0); AT_PK4(p0, 8, pa1); AT_PK4(p1, 0, pa2); AT_PK4(p1, 8, pa3);
.LBB0_400:
	v_add_u32_e32 v67, s0, v171
	ds_read_b128 v[178:181], v67 offset:0
	ds_read_b128 v[182:185], v67 offset:0x1000
	v_add_u32_e32 v72, s0, v199
	ds_read_b128 v[186:189], v72 offset:0
	ds_read_b128 v[190:193], v72 offset:0x1000
	v_add_u32_e32 v73, s0, v200
	ds_read_b128 v[206:209], v73 offset:0
	ds_read_b128 v[210:213], v73 offset:0x1000
	v_exp_f32_e32 v222, v130
	v_add_u32_e32 v130, s0, v201
	ds_read_b128 v[214:217], v130 offset:0
	ds_read_b128 v[218:221], v130 offset:0x1000
	v_exp_f32_e32 v223, v131
	v_exp_f32_e32 v224, v132
	v_exp_f32_e32 v225, v133
	v_exp_f32_e32 v234, v134
	v_exp_f32_e32 v235, v135
	v_exp_f32_e32 v238, v136
	v_exp_f32_e32 v239, v137
	v_exp_f32_e32 v240, v138
	v_exp_f32_e32 v241, v139
	v_exp_f32_e32 v242, v140
	v_exp_f32_e32 v243, v141
	v_exp_f32_e32 v244, v142
	v_exp_f32_e32 v245, v143
	v_exp_f32_e32 v246, v144
	v_exp_f32_e32 v247, v145
	v_mfma_f32_32x32x16_bf16 v[50:65], v[68:71], v[164:167], v[50:65]
	v_mfma_f32_32x32x16_bf16 v[50:65], v[78:81], v[110:113], v[50:65]
	v_mfma_f32_32x32x16_bf16 v[50:65], v[74:77], v[106:109], v[50:65]
	v_mfma_f32_32x32x16_bf16 v[50:65], v[98:101], v[102:105], v[50:65]
	s_waitcnt lgkmcnt(6)
	v_mfma_f32_32x32x16_bf16 v[130:145], v[178:181], v[148:151], v[82:97]
	v_exp_f32_e32 v76, v114
	v_exp_f32_e32 v77, v115
	v_exp_f32_e32 v78, v116
	v_exp_f32_e32 v79, v117
	v_exp_f32_e32 v80, v118
	v_exp_f32_e32 v81, v119
	v_exp_f32_e32 v116, v122
	v_mfma_f32_32x32x16_bf16 v[98:113], v[182:185], v[148:151], v[82:97]
	v_exp_f32_e32 v117, v123
	v_exp_f32_e32 v118, v124
	v_exp_f32_e32 v119, v125
	v_exp_f32_e32 v114, v120
	v_exp_f32_e32 v115, v121
	v_exp_f32_e32 v120, v126
	v_exp_f32_e32 v121, v127
	s_waitcnt lgkmcnt(4)
	v_mfma_f32_32x32x16_bf16 v[130:145], v[186:189], v[152:155], v[130:145]
	v_exp_f32_e32 v122, v128
	v_exp_f32_e32 v123, v129
	v_pk_add_f32 v[68:69], v[222:223], v[224:225]
	v_pk_add_f32 v[70:71], v[240:241], v[242:243]
	v_pk_add_f32 v[72:73], v[78:79], v[76:77]
	v_pk_add_f32 v[74:75], v[118:119], v[116:117]
	v_pk_add_f32 v[68:69], v[234:235], v[68:69]
	v_mfma_f32_32x32x16_bf16 v[98:113], v[190:193], v[152:155], v[98:113]
	v_add_f32_e64 v70, v244, v70
	v_add_f32_e64 v71, v245, v71
	v_add_f32_e64 v72, v80, v72
	v_add_f32_e64 v73, v81, v73
	v_add_f32_e64 v74, v120, v74
	v_add_f32_e64 v75, v121, v75
	v_pk_add_f32 v[68:69], v[238:239], v[68:69]
	v_pk_add_f32 v[70:71], v[246:247], v[70:71]
	v_pk_add_f32 v[72:73], v[114:115], v[72:73]
	v_pk_add_f32 v[74:75], v[122:123], v[74:75]
	s_waitcnt lgkmcnt(2)
	v_mfma_f32_32x32x16_bf16 v[130:145], v[206:209], v[156:159], v[130:145]
	v_add_f32_e64 v68, v68, v70
	v_add_f32_e64 v69, v69, v71
	v_add_f32_e64 v70, v72, v74
	v_add_f32_e64 v71, v73, v75
	v_add_f32_e64 v68, v68, v70
	v_add_f32_e64 v69, v69, v71
	v_pk_add_f32 v[192:193], v[68:69], v[68:69] op_sel:[0,1] op_sel_hi:[1,0]
	v_cvt_pk_bf16_f32 v68, v222, v223
	v_mfma_f32_32x32x16_bf16 v[98:113], v[210:213], v[156:159], v[98:113]
	v_mov_b32_e32 v67, v192
	s_nop 1
	v_permlane32_swap_b32_e32 v192, v67
	v_cvt_pk_bf16_f32 v69, v224, v225
	v_cvt_pk_bf16_f32 v70, v234, v235
	v_cvt_pk_bf16_f32 v71, v238, v239
	v_cvt_pk_bf16_f32 v72, v240, v241
	s_waitcnt lgkmcnt(0)
	v_mfma_f32_32x32x16_bf16 v[130:145], v[214:217], v[160:163], v[130:145]
	v_cvt_pk_bf16_f32 v73, v242, v243
	v_cvt_pk_bf16_f32 v74, v244, v245
	v_cvt_pk_bf16_f32 v75, v246, v247
	v_cvt_pk_bf16_f32 v76, v76, v77
	v_cvt_pk_bf16_f32 v77, v78, v79
	v_cvt_pk_bf16_f32 v78, v80, v81
	v_cvt_pk_bf16_f32 v79, v114, v115
	v_mfma_f32_32x32x16_bf16 v[98:113], v[218:221], v[160:163], v[98:113]
	v_cvt_pk_bf16_f32 v114, v116, v117
	v_cvt_pk_bf16_f32 v115, v118, v119
	v_cvt_pk_bf16_f32 v116, v120, v121
	v_cvt_pk_bf16_f32 v117, v122, v123
	s_and_b64 vcc, exec, s[42:43]
	s_cbranch_vccnz .LBB0_409
	s_cmp_ge_u32 s2, s74
	s_mov_b64 s[8:9], -1
	s_cbranch_scc0 .LBB0_403
	s_waitcnt vmcnt(0) lgkmcnt(0)
	s_mov_b64 s[8:9], 0
